# v9: NSA tile loops - current tile's tile-list LDS read issued right after the tile barrier so it shares the round trip of the DMA block's own LDS read
# baseline (speedup 1.0000x reference)
.LBB0_728:
	s_add_i32 s8, s10, 2
	s_cmp_lt_u32 s8, s95
	s_mov_b64 s[8:9], -1
	s_barrier
	v_mov_b32_e32 v234, s22
	ds_read_b32 v234, v234
	s_cbranch_scc1 .LBB0_730
	s_lshl_b32 s11, s92, 15
	s_mov_b64 s[8:9], 0

.LBB0_732:
	v_readfirstlane_b32 s9, v211
	s_mov_b32 s46, s19
	s_waitcnt lgkmcnt(0)
	v_mov_b32_e32 v4, v234
	s_nop 0
	v_readfirstlane_b32 s8, v4
	s_lshl_b32 s10, s8, 4
	v_subrev_u32_e32 v4, s10, v217
	v_cvt_f32_i32_e32 v4, v4
	s_add_i32 s8, s10, 0x40f
	s_cmp_le_i32 s8, s9
	v_cmp_neq_f32_e64 s[8:9], s4, v40
	v_add_f32_e32 v4, 0xc1780000, v4
	s_nop 0
	v_cndmask_b32_e64 v20, v198, -v40, s[8:9]
	v_fmac_f32_e32 v20, v4, v136
	v_pk_fma_f32 v[18:19], v[154:155], s[24:25], v[20:21] op_sel_hi:[1,1,0]
	v_pk_fma_f32 v[16:17], v[152:153], s[34:35], v[20:21] op_sel_hi:[1,1,0]
	v_pk_fma_f32 v[14:15], v[150:151], s[36:37], v[20:21] op_sel_hi:[1,1,0]
	v_pk_fma_f32 v[12:13], v[148:149], s[38:39], v[20:21] op_sel_hi:[1,1,0]
	v_pk_fma_f32 v[10:11], v[146:147], s[40:41], v[20:21] op_sel_hi:[1,1,0]
	v_pk_fma_f32 v[8:9], v[144:145], s[42:43], v[20:21] op_sel_hi:[1,1,0]
	v_pk_fma_f32 v[6:7], v[142:143], s[44:45], v[20:21] op_sel_hi:[1,1,0]
	v_pk_fma_f32 v[4:5], v[136:137], s[46:47], v[20:21] op_sel_hi:[1,1,0]
	v_pk_fma_f32 v[34:35], v[154:155], s[48:49], v[20:21] op_sel_hi:[1,1,0]
	v_pk_fma_f32 v[32:33], v[152:153], s[50:51], v[20:21] op_sel_hi:[1,1,0]
	v_pk_fma_f32 v[30:31], v[150:151], s[52:53], v[20:21] op_sel_hi:[1,1,0]
	v_pk_fma_f32 v[28:29], v[148:149], s[54:55], v[20:21] op_sel_hi:[1,1,0]
	v_pk_fma_f32 v[26:27], v[146:147], s[56:57], v[20:21] op_sel_hi:[1,1,0]
	v_pk_fma_f32 v[24:25], v[144:145], s[58:59], v[20:21] op_sel_hi:[1,1,0]
	v_pk_fma_f32 v[22:23], v[142:143], s[60:61], v[20:21] op_sel_hi:[1,1,0]
	v_pk_fma_f32 v[20:21], v[136:137], s[62:63], v[20:21] op_sel_hi:[1,1,0]
	v_add_u32_e32 v39, s11, v233
	v_add_u32_e32 v66, v39, v214
	v_add_u32_e32 v41, v39, v213
	v_add_u32_e32 v67, v39, v215
	ds_read_b128 v[42:45], v66 offset:24576
	ds_read_b128 v[46:49], v66 offset:16384
	ds_read_b128 v[50:53], v67 offset:16384
	ds_read_b128 v[54:57], v67 offset:24576
	ds_read_b128 v[58:61], v41 offset:24576
	ds_read_b128 v[62:65], v41 offset:16384
	v_add_u32_e32 v39, v39, v216
	s_waitcnt lgkmcnt(0)
	v_mfma_f32_32x32x16_bf16 v[4:19], v[62:65], v[100:103], v[4:19]
	v_mfma_f32_32x32x16_bf16 v[20:35], v[58:61], v[100:103], v[20:35]
	ds_read_b128 v[58:61], v39 offset:16384
	ds_read_b128 v[62:65], v39 offset:24576
	v_mfma_f32_32x32x16_bf16 v[4:19], v[46:49], v[104:107], v[4:19]
	v_mfma_f32_32x32x16_bf16 v[20:35], v[42:45], v[104:107], v[20:35]
	ds_read_b128 v[42:45], v41 offset:16512
	ds_read_b128 v[46:49], v41 offset:24704
	v_mfma_f32_32x32x16_bf16 v[4:19], v[50:53], v[108:111], v[4:19]
	v_mfma_f32_32x32x16_bf16 v[20:35], v[54:57], v[108:111], v[20:35]
	ds_read_b128 v[50:53], v66 offset:16512
	ds_read_b128 v[54:57], v66 offset:24704
	s_waitcnt lgkmcnt(0)
	v_mfma_f32_32x32x16_bf16 v[4:19], v[58:61], v[112:115], v[4:19]
	v_mfma_f32_32x32x16_bf16 v[20:35], v[62:65], v[112:115], v[20:35]
	ds_read_b128 v[58:61], v67 offset:16512
	ds_read_b128 v[62:65], v67 offset:24704
	v_mfma_f32_32x32x16_bf16 v[4:19], v[42:45], v[116:119], v[4:19]
	v_mfma_f32_32x32x16_bf16 v[20:35], v[46:49], v[116:119], v[20:35]
	ds_read_b128 v[42:45], v39 offset:16512
	ds_read_b128 v[46:49], v39 offset:24704
	v_mfma_f32_32x32x16_bf16 v[4:19], v[50:53], v[120:123], v[4:19]
	v_mfma_f32_32x32x16_bf16 v[20:35], v[54:57], v[120:123], v[20:35]
	s_waitcnt lgkmcnt(0)
	v_mfma_f32_32x32x16_bf16 v[4:19], v[58:61], v[124:127], v[4:19]
	v_mfma_f32_32x32x16_bf16 v[20:35], v[62:65], v[124:127], v[20:35]
	v_mfma_f32_32x32x16_bf16 v[4:19], v[42:45], v[128:131], v[4:19]
	v_mfma_f32_32x32x16_bf16 v[20:35], v[46:49], v[128:131], v[20:35]
	s_cbranch_scc1 .LBB0_734
	v_subrev_u32_e32 v39, s10, v185
	v_add_u32_e32 v39, v39, v212
	v_cmp_lt_i32_e32 vcc, 30, v39
	s_nop 6
	v_cndmask_b32_e32 v4, v199, v4, vcc
	v_cmp_lt_i32_e32 vcc, s5, v39
	v_subrev_u32_e32 v39, s10, v218
	s_nop 0
	v_cndmask_b32_e32 v20, v199, v20, vcc
	v_cmp_lt_i32_e32 vcc, 30, v39
	s_nop 1
	v_cndmask_b32_e32 v5, v199, v5, vcc
	v_cmp_lt_i32_e32 vcc, s5, v39
	v_subrev_u32_e32 v39, s10, v219
	s_nop 0
	v_cndmask_b32_e32 v21, v199, v21, vcc
	v_cmp_lt_i32_e32 vcc, 30, v39
	s_nop 1
	v_cndmask_b32_e32 v6, v199, v6, vcc
	v_cmp_lt_i32_e32 vcc, s5, v39
	v_subrev_u32_e32 v39, s10, v220
	s_nop 0
	v_cndmask_b32_e32 v22, v199, v22, vcc
	v_cmp_lt_i32_e32 vcc, 30, v39
	s_nop 1
	v_cndmask_b32_e32 v7, v199, v7, vcc
	v_cmp_lt_i32_e32 vcc, s5, v39
	v_subrev_u32_e32 v39, s10, v221
	s_nop 0
	v_cndmask_b32_e32 v23, v199, v23, vcc
	v_cmp_lt_i32_e32 vcc, 30, v39
	s_nop 1
	v_cndmask_b32_e32 v8, v199, v8, vcc
	v_cmp_lt_i32_e32 vcc, s5, v39
	v_subrev_u32_e32 v39, s10, v222
	s_nop 0
	v_cndmask_b32_e32 v24, v199, v24, vcc
	v_cmp_lt_i32_e32 vcc, 30, v39
	s_nop 1
	v_cndmask_b32_e32 v9, v199, v9, vcc
	v_cmp_lt_i32_e32 vcc, s5, v39
	v_subrev_u32_e32 v39, s10, v223
	s_nop 0
	v_cndmask_b32_e32 v25, v199, v25, vcc
	v_cmp_lt_i32_e32 vcc, 30, v39
	s_nop 1
	v_cndmask_b32_e32 v10, v199, v10, vcc
	v_cmp_lt_i32_e32 vcc, s5, v39
	v_subrev_u32_e32 v39, s10, v224
	s_nop 0
	v_cndmask_b32_e32 v26, v199, v26, vcc
	v_cmp_lt_i32_e32 vcc, 30, v39
	s_nop 1
	v_cndmask_b32_e32 v11, v199, v11, vcc
	v_cmp_lt_i32_e32 vcc, s5, v39
	v_subrev_u32_e32 v39, s10, v225
	s_nop 0
	v_cndmask_b32_e32 v27, v199, v27, vcc
	v_cmp_lt_i32_e32 vcc, 30, v39
	s_nop 1
	v_cndmask_b32_e32 v12, v199, v12, vcc
	v_cmp_lt_i32_e32 vcc, s5, v39
	v_subrev_u32_e32 v39, s10, v226
	s_nop 0
	v_cndmask_b32_e32 v28, v199, v28, vcc
	v_cmp_lt_i32_e32 vcc, 30, v39
	s_nop 1
	v_cndmask_b32_e32 v13, v199, v13, vcc
	v_cmp_lt_i32_e32 vcc, s5, v39
	v_subrev_u32_e32 v39, s10, v227
	s_nop 0
	v_cndmask_b32_e32 v29, v199, v29, vcc
	v_cmp_lt_i32_e32 vcc, 30, v39
	s_nop 1
	v_cndmask_b32_e32 v14, v199, v14, vcc
	v_cmp_lt_i32_e32 vcc, s5, v39
	v_subrev_u32_e32 v39, s10, v228
	s_nop 0
	v_cndmask_b32_e32 v30, v199, v30, vcc
	v_cmp_lt_i32_e32 vcc, 30, v39
	s_nop 1
	v_cndmask_b32_e32 v15, v199, v15, vcc
	v_cmp_lt_i32_e32 vcc, s5, v39
	v_subrev_u32_e32 v39, s10, v229
	s_nop 0
	v_cndmask_b32_e32 v31, v199, v31, vcc
	v_cmp_lt_i32_e32 vcc, 30, v39
	s_nop 1
	v_cndmask_b32_e32 v16, v199, v16, vcc
	v_cmp_lt_i32_e32 vcc, s5, v39
	v_subrev_u32_e32 v39, s10, v230
	s_nop 0
	v_cndmask_b32_e32 v32, v199, v32, vcc
	v_cmp_lt_i32_e32 vcc, 30, v39
	s_nop 1
	v_cndmask_b32_e32 v17, v199, v17, vcc
	v_cmp_lt_i32_e32 vcc, s5, v39
	v_subrev_u32_e32 v39, s10, v231
	s_nop 0
	v_cndmask_b32_e32 v33, v199, v33, vcc
	v_cmp_lt_i32_e32 vcc, 30, v39
	s_nop 1
	v_cndmask_b32_e32 v18, v199, v18, vcc
	v_cmp_lt_i32_e32 vcc, s5, v39
	v_subrev_u32_e32 v39, s10, v232
	s_nop 0
	v_cndmask_b32_e32 v34, v199, v34, vcc
	v_cmp_lt_i32_e32 vcc, 30, v39
	s_nop 1
	v_cndmask_b32_e32 v19, v199, v19, vcc
	v_cmp_lt_i32_e32 vcc, s5, v39
	s_nop 1
	v_cndmask_b32_e32 v35, v199, v35, vcc

.LBB0_744:
	s_add_i32 s2, s6, 2
	s_cmp_lt_u32 s2, s95
	s_mov_b64 s[2:3], -1
	s_barrier
	v_mov_b32_e32 v242, s92
	ds_read_b32 v242, v242
	s_cbranch_scc1 .LBB0_746
	s_lshl_b32 s22, s93, 15
	s_mov_b64 s[2:3], 0

.LBB0_748:
	s_mov_b32 s46, s19
	v_readfirstlane_b32 s3, v211
	s_waitcnt lgkmcnt(0)
	v_mov_b32_e32 v235, v242
	s_nop 0
	v_readfirstlane_b32 s2, v235
	s_lshl_b32 s2, s2, 4
	s_nop 0
	v_subrev_u32_e32 v68, s2, v217
	v_cvt_f32_i32_e32 v68, v68
	s_add_i32 s6, s2, 0x40f
	s_cmp_le_i32 s6, s3
	v_add_f32_e32 v68, 0xc1780000, v68
	v_fma_f32 v84, v68, v136, v2
	v_pk_fma_f32 v[82:83], v[154:155], s[24:25], v[84:85] op_sel_hi:[1,1,0]
	v_pk_fma_f32 v[80:81], v[152:153], s[34:35], v[84:85] op_sel_hi:[1,1,0]
	v_pk_fma_f32 v[78:79], v[150:151], s[36:37], v[84:85] op_sel_hi:[1,1,0]
	v_pk_fma_f32 v[76:77], v[148:149], s[38:39], v[84:85] op_sel_hi:[1,1,0]
	v_pk_fma_f32 v[74:75], v[146:147], s[40:41], v[84:85] op_sel_hi:[1,1,0]
	v_pk_fma_f32 v[72:73], v[144:145], s[42:43], v[84:85] op_sel_hi:[1,1,0]
	v_pk_fma_f32 v[70:71], v[142:143], s[44:45], v[84:85] op_sel_hi:[1,1,0]
	v_pk_fma_f32 v[68:69], v[136:137], s[46:47], v[84:85] op_sel_hi:[1,1,0]
	v_pk_fma_f32 v[98:99], v[154:155], s[48:49], v[84:85] op_sel_hi:[1,1,0]
	v_pk_fma_f32 v[96:97], v[152:153], s[50:51], v[84:85] op_sel_hi:[1,1,0]
	v_pk_fma_f32 v[94:95], v[150:151], s[52:53], v[84:85] op_sel_hi:[1,1,0]
	v_pk_fma_f32 v[92:93], v[148:149], s[54:55], v[84:85] op_sel_hi:[1,1,0]
	v_pk_fma_f32 v[90:91], v[146:147], s[56:57], v[84:85] op_sel_hi:[1,1,0]
	v_pk_fma_f32 v[88:89], v[144:145], s[58:59], v[84:85] op_sel_hi:[1,1,0]
	v_pk_fma_f32 v[86:87], v[142:143], s[60:61], v[84:85] op_sel_hi:[1,1,0]
	v_pk_fma_f32 v[84:85], v[136:137], s[62:63], v[84:85] op_sel_hi:[1,1,0]
	v_add_u32_e32 v158, s22, v233
	v_add_u32_e32 v183, v158, v214
	v_add_u32_e32 v182, v158, v213
	v_add_u32_e32 v236, v158, v215
	v_add_u32_e32 v237, v158, v216
	ds_read_b128 v[158:161], v183 offset:24576
	ds_read_b128 v[162:165], v183 offset:16384
	ds_read_b128 v[166:169], v236 offset:16384
	ds_read_b128 v[170:173], v236 offset:24576
	ds_read_b128 v[174:177], v182 offset:24576
	ds_read_b128 v[178:181], v182 offset:16384
	s_waitcnt lgkmcnt(0)
	v_mfma_f32_32x32x16_bf16 v[68:83], v[178:181], v[100:103], v[68:83]
	v_mfma_f32_32x32x16_bf16 v[84:99], v[174:177], v[100:103], v[84:99]
	ds_read_b128 v[174:177], v237 offset:16384
	ds_read_b128 v[178:181], v237 offset:24576
	v_mfma_f32_32x32x16_bf16 v[68:83], v[162:165], v[104:107], v[68:83]
	v_mfma_f32_32x32x16_bf16 v[84:99], v[158:161], v[104:107], v[84:99]
	ds_read_b128 v[158:161], v182 offset:16512
	ds_read_b128 v[162:165], v182 offset:24704
	v_mfma_f32_32x32x16_bf16 v[68:83], v[166:169], v[108:111], v[68:83]
	v_mfma_f32_32x32x16_bf16 v[84:99], v[170:173], v[108:111], v[84:99]
	ds_read_b128 v[166:169], v183 offset:16512
	ds_read_b128 v[170:173], v183 offset:24704
	s_waitcnt lgkmcnt(0)
	v_mfma_f32_32x32x16_bf16 v[68:83], v[174:177], v[112:115], v[68:83]
	v_mfma_f32_32x32x16_bf16 v[84:99], v[178:181], v[112:115], v[84:99]
	ds_read_b128 v[174:177], v236 offset:16512
	ds_read_b128 v[178:181], v236 offset:24704
	v_mfma_f32_32x32x16_bf16 v[68:83], v[158:161], v[116:119], v[68:83]
	v_mfma_f32_32x32x16_bf16 v[84:99], v[162:165], v[116:119], v[84:99]
	ds_read_b128 v[158:161], v237 offset:16512
	ds_read_b128 v[162:165], v237 offset:24704
	v_mfma_f32_32x32x16_bf16 v[68:83], v[166:169], v[120:123], v[68:83]
	v_mfma_f32_32x32x16_bf16 v[84:99], v[170:173], v[120:123], v[84:99]
	s_waitcnt lgkmcnt(0)
	v_mfma_f32_32x32x16_bf16 v[68:83], v[174:177], v[124:127], v[68:83]
	v_mfma_f32_32x32x16_bf16 v[84:99], v[178:181], v[124:127], v[84:99]
	v_mfma_f32_32x32x16_bf16 v[68:83], v[158:161], v[128:131], v[68:83]
	v_mfma_f32_32x32x16_bf16 v[84:99], v[162:165], v[128:131], v[84:99]
	s_cbranch_scc1 .LBB0_750
	v_subrev_u32_e32 v158, s2, v185
	v_add_u32_e32 v158, v158, v212
	v_cmp_lt_i32_e32 vcc, 30, v158
	s_nop 6
	v_cndmask_b32_e32 v68, v199, v68, vcc
	v_cmp_lt_i32_e32 vcc, s5, v158
	v_subrev_u32_e32 v158, s2, v218
	s_nop 0
	v_cndmask_b32_e32 v84, v199, v84, vcc
	v_cmp_lt_i32_e32 vcc, 30, v158
	s_nop 1
	v_cndmask_b32_e32 v69, v199, v69, vcc
	v_cmp_lt_i32_e32 vcc, s5, v158
	v_subrev_u32_e32 v158, s2, v219
	s_nop 0
	v_cndmask_b32_e32 v85, v199, v85, vcc
	v_cmp_lt_i32_e32 vcc, 30, v158
	s_nop 1
	v_cndmask_b32_e32 v70, v199, v70, vcc
	v_cmp_lt_i32_e32 vcc, s5, v158
	v_subrev_u32_e32 v158, s2, v220
	s_nop 0
	v_cndmask_b32_e32 v86, v199, v86, vcc
	v_cmp_lt_i32_e32 vcc, 30, v158
	s_nop 1
	v_cndmask_b32_e32 v71, v199, v71, vcc
	v_cmp_lt_i32_e32 vcc, s5, v158
	v_subrev_u32_e32 v158, s2, v221
	s_nop 0
	v_cndmask_b32_e32 v87, v199, v87, vcc
	v_cmp_lt_i32_e32 vcc, 30, v158
	s_nop 1
	v_cndmask_b32_e32 v72, v199, v72, vcc
	v_cmp_lt_i32_e32 vcc, s5, v158
	v_subrev_u32_e32 v158, s2, v222
	s_nop 0
	v_cndmask_b32_e32 v88, v199, v88, vcc
	v_cmp_lt_i32_e32 vcc, 30, v158
	s_nop 1
	v_cndmask_b32_e32 v73, v199, v73, vcc
	v_cmp_lt_i32_e32 vcc, s5, v158
	v_subrev_u32_e32 v158, s2, v223
	s_nop 0
	v_cndmask_b32_e32 v89, v199, v89, vcc
	v_cmp_lt_i32_e32 vcc, 30, v158
	s_nop 1
	v_cndmask_b32_e32 v74, v199, v74, vcc
	v_cmp_lt_i32_e32 vcc, s5, v158
	v_subrev_u32_e32 v158, s2, v224
	s_nop 0
	v_cndmask_b32_e32 v90, v199, v90, vcc
	v_cmp_lt_i32_e32 vcc, 30, v158
	s_nop 1
	v_cndmask_b32_e32 v75, v199, v75, vcc
	v_cmp_lt_i32_e32 vcc, s5, v158
	v_subrev_u32_e32 v158, s2, v225
	s_nop 0
	v_cndmask_b32_e32 v91, v199, v91, vcc
	v_cmp_lt_i32_e32 vcc, 30, v158
	s_nop 1
	v_cndmask_b32_e32 v76, v199, v76, vcc
	v_cmp_lt_i32_e32 vcc, s5, v158
	v_subrev_u32_e32 v158, s2, v226
	s_nop 0
	v_cndmask_b32_e32 v92, v199, v92, vcc
	v_cmp_lt_i32_e32 vcc, 30, v158
	s_nop 1
	v_cndmask_b32_e32 v77, v199, v77, vcc
	v_cmp_lt_i32_e32 vcc, s5, v158
	v_subrev_u32_e32 v158, s2, v227
	s_nop 0
	v_cndmask_b32_e32 v93, v199, v93, vcc
	v_cmp_lt_i32_e32 vcc, 30, v158
	s_nop 1
	v_cndmask_b32_e32 v78, v199, v78, vcc
	v_cmp_lt_i32_e32 vcc, s5, v158
	v_subrev_u32_e32 v158, s2, v228
	s_nop 0
	v_cndmask_b32_e32 v94, v199, v94, vcc
	v_cmp_lt_i32_e32 vcc, 30, v158
	s_nop 1
	v_cndmask_b32_e32 v79, v199, v79, vcc
	v_cmp_lt_i32_e32 vcc, s5, v158
	v_subrev_u32_e32 v158, s2, v229
	s_nop 0
	v_cndmask_b32_e32 v95, v199, v95, vcc
	v_cmp_lt_i32_e32 vcc, 30, v158
	s_nop 1
	v_cndmask_b32_e32 v80, v199, v80, vcc
	v_cmp_lt_i32_e32 vcc, s5, v158
	v_subrev_u32_e32 v158, s2, v230
	s_nop 0
	v_cndmask_b32_e32 v96, v199, v96, vcc
	v_cmp_lt_i32_e32 vcc, 30, v158
	s_nop 1
	v_cndmask_b32_e32 v81, v199, v81, vcc
	v_cmp_lt_i32_e32 vcc, s5, v158
	v_subrev_u32_e32 v158, s2, v231
	s_nop 0
	v_cndmask_b32_e32 v97, v199, v97, vcc
	v_cmp_lt_i32_e32 vcc, 30, v158
	s_nop 1
	v_cndmask_b32_e32 v82, v199, v82, vcc
	v_cmp_lt_i32_e32 vcc, s5, v158
	v_subrev_u32_e32 v158, s2, v232
	s_nop 0
	v_cndmask_b32_e32 v98, v199, v98, vcc
	v_cmp_lt_i32_e32 vcc, 30, v158
	s_nop 1
	v_cndmask_b32_e32 v83, v199, v83, vcc
	v_cmp_lt_i32_e32 vcc, s5, v158
	s_nop 1
	v_cndmask_b32_e32 v99, v199, v99, vcc

.LBB0_789:
	s_add_i32 s2, s7, 2
	s_cmp_le_i32 s2, s64
	s_mov_b64 s[2:3], -1
	s_barrier
	v_mov_b32_e32 v227, s17
	ds_read_b32 v227, v227
	s_cbranch_scc0 .LBB0_791
	v_mov_b32_e32 v2, s17
	ds_read_b32 v2, v2 offset:8
	s_lshl_b32 s22, s6, 15
	s_add_i32 s2, s22, 0xffff8000
	s_cmp_lg_u32 s6, 0
	s_cselect_b32 s10, s2, 0x10000
	s_waitcnt lgkmcnt(0)
	v_add_u32_e32 v70, v2, v189
	v_add_u32_e32 v68, v70, v158
	s_add_i32 s10, s46, s10
	v_mad_i64_i32 v[68:69], s[2:3], v68, s76, v[132:133]
	s_mov_b32 m0, s10
	s_nop 0
	global_load_lds_dwordx4 v[68:69], off
	v_add_u32_e32 v68, v2, v188
	v_mad_i64_i32 v[68:69], s[2:3], v68, s76, v[134:135]
	s_add_i32 m0, s10, 0x4000
	v_add_u32_e32 v2, v2, v159
	global_load_lds_dwordx4 v[68:69], off
	v_add_u32_e32 v68, v70, v160
	v_mad_i64_i32 v[68:69], s[2:3], v68, s76, v[132:133]
	s_add_i32 m0, s10, 0x2000
	s_nop 0
	global_load_lds_dwordx4 v[68:69], off
	v_mad_i64_i32 v[68:69], s[2:3], v2, s76, v[142:143]
	s_add_i32 m0, s10, 0x6000
	s_mov_b64 s[2:3], 0
	global_load_lds_dwordx4 v[68:69], off

.LBB0_793:
	v_readfirstlane_b32 s2, v178
	s_waitcnt lgkmcnt(0)
	v_mov_b32_e32 v2, v227
	s_nop 0
	v_add_u32_e32 v68, 63, v2
	v_cmp_lt_i32_e32 vcc, s2, v68
	s_mov_b64 s[2:3], -1
	s_cbranch_vccnz .LBB0_795
	v_readfirstlane_b32 s2, v178
	s_addk_i32 s2, 0xfe08
	s_nop 0
	v_cmp_gt_i32_e64 s[2:3], s2, v2

.LBB0_972:
	s_add_i32 s2, s10, 2
	s_cmp_lt_i32 s2, s17
	s_mov_b64 s[2:3], -1
	s_barrier
	v_mov_b32_e32 v243, s23
	ds_read_b32 v243, v243
	s_cbranch_scc1 .LBB0_974
	s_lshl_b32 s70, s22, 15
	s_mov_b64 s[2:3], 0

.LBB0_976:
	s_movk_i32 s2, 0x800
	v_cmp_neq_f32_e64 s[10:11], s4, v212
	s_mov_b32 s26, s47
	s_mov_b32 s28, s45
	s_waitcnt lgkmcnt(0)
	v_mov_b32_e32 v2, v243
	s_nop 0
	v_ashrrev_i32_e32 v69, 11, v2
	v_cmp_eq_u32_e32 vcc, 2, v69
	v_lshrrev_b32_e32 v68, 6, v2
	s_mov_b32 s30, s44
	v_cndmask_b32_e32 v70, v135, v134, vcc
	v_cmp_eq_u32_e32 vcc, 1, v69
	s_nop 1
	v_cndmask_b32_e32 v69, v70, v133, vcc
	v_cmp_gt_u32_e32 vcc, s2, v2
	v_add_u32_e32 v70, 63, v2
	v_add_u32_e32 v2, v2, v206
	v_sub_u32_e32 v214, v185, v2
	v_cvt_f32_i32_e32 v71, v214
	v_cndmask_b32_e32 v69, v69, v132, vcc
	v_readfirstlane_b32 s2, v205
	v_lshrrev_b32_e32 v68, v68, v69
	v_and_b32_e32 v68, 1, v68
	v_cmp_ge_i32_e32 vcc, s2, v70
	v_cndmask_b32_e64 v70, v198, -v212, s[10:11]
	v_fmac_f32_e32 v70, v71, v136
	v_cmp_eq_u32_e64 s[12:13], 1, v68
	s_mov_b32 s2, -2.0
	s_mov_b32 s3, 0xc0400000
	v_cndmask_b32_e64 v84, v199, v70, s[12:13]
	v_pk_fma_f32 v[70:71], v[136:137], s[2:3], v[84:85] op_sel_hi:[1,1,0]
	s_mov_b32 s2, 0xc1000000
	s_mov_b32 s3, 0xc1100000
	v_pk_fma_f32 v[72:73], v[136:137], s[2:3], v[84:85] op_sel_hi:[1,1,0]
	s_mov_b32 s2, 0xc1200000
	s_mov_b32 s3, 0xc1300000
	v_pk_fma_f32 v[74:75], v[136:137], s[2:3], v[84:85] op_sel_hi:[1,1,0]
	s_mov_b32 s2, 0xc1900000
	s_mov_b32 s3, 0xc1980000
	v_pk_fma_f32 v[78:79], v[136:137], s[2:3], v[84:85] op_sel_hi:[1,1,0]
	s_mov_b32 s2, 0xc1c00000
	s_mov_b32 s3, 0xc1c80000
	v_pk_fma_f32 v[80:81], v[136:137], s[2:3], v[84:85] op_sel_hi:[1,1,0]
	s_mov_b32 s2, 0xc1d00000
	s_mov_b32 s3, 0xc1d80000
	v_pk_fma_f32 v[82:83], v[136:137], s[2:3], v[84:85] op_sel_hi:[1,1,0]
	s_mov_b32 s2, 0xc2680000
	s_mov_b32 s3, 0xc26c0000
	v_pk_fma_f32 v[98:99], v[162:163], s[2:3], v[84:85] op_sel_hi:[1,1,0]
	s_mov_b32 s2, 0xc2600000
	s_mov_b32 s3, 0xc2640000
	v_pk_fma_f32 v[96:97], v[160:161], s[2:3], v[84:85] op_sel_hi:[1,1,0]
	s_mov_b32 s2, 0xc2480000
	s_mov_b32 s3, 0xc24c0000
	v_pk_fma_f32 v[94:95], v[158:159], s[2:3], v[84:85] op_sel_hi:[1,1,0]
	s_mov_b32 s2, 0xc2280000
	s_mov_b32 s3, 0xc22c0000
	v_fma_f32 v68, 0, v136, v84
	v_sub_f32_e32 v69, v84, v136
	v_pk_fma_f32 v[76:77], v[136:137], s[26:27], v[84:85] op_sel_hi:[1,1,0]
	v_pk_fma_f32 v[92:93], v[156:157], s[28:29], v[84:85] op_sel_hi:[1,1,0]
	v_pk_fma_f32 v[90:91], v[154:155], s[2:3], v[84:85] op_sel_hi:[1,1,0]
	v_pk_fma_f32 v[88:89], v[152:153], s[0:1], v[84:85] op_sel_hi:[1,1,0]
	v_pk_fma_f32 v[86:87], v[150:151], s[20:21], v[84:85] op_sel_hi:[1,1,0]
	v_pk_fma_f32 v[84:85], v[148:149], s[30:31], v[84:85] op_sel_hi:[1,1,0]
	v_add_u32_e32 v215, s70, v211
	v_add_u32_e32 v241, v215, v208
	v_add_u32_e32 v240, v215, v207
	v_add_u32_e32 v242, v215, v209
	ds_read_b128 v[216:219], v241 offset:24576
	ds_read_b128 v[220:223], v241 offset:16384
	ds_read_b128 v[224:227], v242 offset:16384
	ds_read_b128 v[228:231], v242 offset:24576
	ds_read_b128 v[232:235], v240 offset:24576
	ds_read_b128 v[236:239], v240 offset:16384
	v_add_u32_e32 v215, v215, v210
	s_waitcnt lgkmcnt(0)
	v_mfma_f32_32x32x16_bf16 v[68:83], v[236:239], v[100:103], v[68:83]
	v_mfma_f32_32x32x16_bf16 v[84:99], v[232:235], v[100:103], v[84:99]
	ds_read_b128 v[232:235], v215 offset:16384
	ds_read_b128 v[236:239], v215 offset:24576
	v_mfma_f32_32x32x16_bf16 v[68:83], v[220:223], v[104:107], v[68:83]
	v_mfma_f32_32x32x16_bf16 v[84:99], v[216:219], v[104:107], v[84:99]
	ds_read_b128 v[216:219], v240 offset:16512
	ds_read_b128 v[220:223], v240 offset:24704
	v_mfma_f32_32x32x16_bf16 v[68:83], v[224:227], v[108:111], v[68:83]
	v_mfma_f32_32x32x16_bf16 v[84:99], v[228:231], v[108:111], v[84:99]
	ds_read_b128 v[224:227], v241 offset:16512
	ds_read_b128 v[228:231], v241 offset:24704
	s_waitcnt lgkmcnt(0)
	v_mfma_f32_32x32x16_bf16 v[68:83], v[232:235], v[112:115], v[68:83]
	v_mfma_f32_32x32x16_bf16 v[84:99], v[236:239], v[112:115], v[84:99]
	ds_read_b128 v[232:235], v242 offset:16512
	ds_read_b128 v[236:239], v242 offset:24704
	v_mfma_f32_32x32x16_bf16 v[68:83], v[216:219], v[116:119], v[68:83]
	v_mfma_f32_32x32x16_bf16 v[84:99], v[220:223], v[116:119], v[84:99]
	ds_read_b128 v[216:219], v215 offset:16512
	ds_read_b128 v[220:223], v215 offset:24704
	v_mfma_f32_32x32x16_bf16 v[68:83], v[224:227], v[120:123], v[68:83]
	v_mfma_f32_32x32x16_bf16 v[84:99], v[228:231], v[120:123], v[84:99]
	s_waitcnt lgkmcnt(0)
	v_mfma_f32_32x32x16_bf16 v[68:83], v[232:235], v[124:127], v[68:83]
	v_mfma_f32_32x32x16_bf16 v[84:99], v[236:239], v[124:127], v[84:99]
	v_mfma_f32_32x32x16_bf16 v[68:83], v[216:219], v[128:131], v[68:83]
	v_mfma_f32_32x32x16_bf16 v[84:99], v[220:223], v[128:131], v[84:99]
	s_cbranch_vccnz .LBB0_978
	v_cmp_lt_i32_e32 vcc, -1, v214
	s_nop 8
	v_cndmask_b32_e32 v68, v199, v68, vcc
	v_cmp_lt_i32_e32 vcc, 31, v214
	v_xad_u32 v214, v2, -1, v185
	s_nop 0
	v_cndmask_b32_e32 v84, v199, v84, vcc
	v_cmp_lt_i32_e32 vcc, -1, v214
	s_nop 1
	v_cndmask_b32_e32 v69, v199, v69, vcc
	v_cmp_lt_i32_e32 vcc, 31, v214
	v_sub_u32_e32 v214, v170, v2
	s_nop 0
	v_cndmask_b32_e32 v85, v199, v85, vcc
	v_cmp_lt_i32_e32 vcc, -1, v214
	s_nop 1
	v_cndmask_b32_e32 v70, v199, v70, vcc
	v_cmp_lt_i32_e32 vcc, 31, v214
	v_sub_u32_e32 v214, v171, v2
	s_nop 0
	v_cndmask_b32_e32 v86, v199, v86, vcc
	v_cmp_lt_i32_e32 vcc, -1, v214
	s_nop 1
	v_cndmask_b32_e32 v71, v199, v71, vcc
	v_cmp_lt_i32_e32 vcc, 31, v214
	v_sub_u32_e32 v214, v172, v2
	s_nop 0
	v_cndmask_b32_e32 v87, v199, v87, vcc
	v_cmp_lt_i32_e32 vcc, -1, v214
	s_nop 1
	v_cndmask_b32_e32 v72, v199, v72, vcc
	v_cmp_lt_i32_e32 vcc, 31, v214
	v_sub_u32_e32 v214, v173, v2
	s_nop 0
	v_cndmask_b32_e32 v88, v199, v88, vcc
	v_cmp_lt_i32_e32 vcc, -1, v214
	s_nop 1
	v_cndmask_b32_e32 v73, v199, v73, vcc
	v_cmp_lt_i32_e32 vcc, 31, v214
	v_sub_u32_e32 v214, v174, v2
	s_nop 0
	v_cndmask_b32_e32 v89, v199, v89, vcc
	v_cmp_lt_i32_e32 vcc, -1, v214
	s_nop 1
	v_cndmask_b32_e32 v74, v199, v74, vcc
	v_cmp_lt_i32_e32 vcc, 31, v214
	v_sub_u32_e32 v214, v175, v2
	s_nop 0
	v_cndmask_b32_e32 v90, v199, v90, vcc
	v_cmp_lt_i32_e32 vcc, -1, v214
	s_nop 1
	v_cndmask_b32_e32 v75, v199, v75, vcc
	v_cmp_lt_i32_e32 vcc, 31, v214
	v_sub_u32_e32 v214, v176, v2
	s_nop 0
	v_cndmask_b32_e32 v91, v199, v91, vcc
	v_cmp_lt_i32_e32 vcc, -1, v214
	s_nop 1
	v_cndmask_b32_e32 v76, v199, v76, vcc
	v_cmp_lt_i32_e32 vcc, 31, v214
	v_sub_u32_e32 v214, v177, v2
	s_nop 0
	v_cndmask_b32_e32 v92, v199, v92, vcc
	v_cmp_lt_i32_e32 vcc, -1, v214
	s_nop 1
	v_cndmask_b32_e32 v77, v199, v77, vcc
	v_cmp_lt_i32_e32 vcc, 31, v214
	v_sub_u32_e32 v214, v178, v2
	s_nop 0
	v_cndmask_b32_e32 v93, v199, v93, vcc
	v_cmp_lt_i32_e32 vcc, -1, v214
	s_nop 1
	v_cndmask_b32_e32 v78, v199, v78, vcc
	v_cmp_lt_i32_e32 vcc, 31, v214
	v_sub_u32_e32 v214, v179, v2
	s_nop 0
	v_cndmask_b32_e32 v94, v199, v94, vcc
	v_cmp_lt_i32_e32 vcc, -1, v214
	s_nop 1
	v_cndmask_b32_e32 v79, v199, v79, vcc
	v_cmp_lt_i32_e32 vcc, 31, v214
	v_sub_u32_e32 v214, v180, v2
	s_nop 0
	v_cndmask_b32_e32 v95, v199, v95, vcc
	v_cmp_lt_i32_e32 vcc, -1, v214
	s_nop 1
	v_cndmask_b32_e32 v80, v199, v80, vcc
	v_cmp_lt_i32_e32 vcc, 31, v214
	v_sub_u32_e32 v214, v181, v2
	s_nop 0
	v_cndmask_b32_e32 v96, v199, v96, vcc
	v_cmp_lt_i32_e32 vcc, -1, v214
	s_nop 1
	v_cndmask_b32_e32 v81, v199, v81, vcc
	v_cmp_lt_i32_e32 vcc, 31, v214
	v_sub_u32_e32 v214, v182, v2
	v_sub_u32_e32 v2, v183, v2
	v_cndmask_b32_e32 v97, v199, v97, vcc
	v_cmp_lt_i32_e32 vcc, -1, v214
	s_nop 1
	v_cndmask_b32_e32 v82, v199, v82, vcc
	v_cmp_lt_i32_e32 vcc, 31, v214
	s_nop 1
	v_cndmask_b32_e32 v98, v199, v98, vcc
	v_cmp_lt_i32_e32 vcc, -1, v2
	s_nop 1
	v_cndmask_b32_e32 v83, v199, v83, vcc
	v_cmp_lt_i32_e32 vcc, 31, v2
	s_nop 1
	v_cndmask_b32_e32 v99, v199, v99, vcc
